# stack: router MFMA-stage loads 24 deep + phase-1 light-job load batching on top of v31
# baseline (speedup 1.0000x reference)
.LBB0_1343:
	s_and_saveexec_b64 s[8:9], s[2:3]
	ds_write_b32 v53, v97
	s_or_b64 exec, exec, s[8:9]
	s_waitcnt vmcnt(0)
	s_waitcnt lgkmcnt(0)
	s_barrier
	global_load_dwordx4 v[100:103], v[56:57], off offset:-256
	global_load_dwordx4 v[104:107], v[16:17], off
	global_load_dwordx4 v[108:111], v[18:19], off
	global_load_dwordx4 v[112:115], v[56:57], off offset:-224
	global_load_dwordx4 v[116:119], v[16:17], off offset:32
	global_load_dwordx4 v[120:123], v[20:21], off
	global_load_dwordx4 v[124:127], v[56:57], off offset:-192
	global_load_dwordx4 v[128:131], v[16:17], off offset:64
	global_load_dwordx4 v[132:135], v[22:23], off
	global_load_dwordx4 v[136:139], v[56:57], off offset:-160
	global_load_dwordx4 v[140:143], v[16:17], off offset:96
	global_load_dwordx4 v[144:147], v[24:25], off
	global_load_dwordx4 v[148:151], v[56:57], off offset:-128
	global_load_dwordx4 v[152:155], v[16:17], off offset:128
	global_load_dwordx4 v[156:159], v[26:27], off
	global_load_dwordx4 v[160:163], v[56:57], off offset:-96
	global_load_dwordx4 v[164:167], v[16:17], off offset:160
	global_load_dwordx4 v[168:171], v[28:29], off
	global_load_dwordx4 v[172:175], v[56:57], off offset:-64
	global_load_dwordx4 v[176:179], v[16:17], off offset:192
	global_load_dwordx4 v[180:183], v[30:31], off
	global_load_dwordx4 v[184:187], v[56:57], off offset:-32
	global_load_dwordx4 v[188:191], v[16:17], off offset:224
	global_load_dwordx4 v[192:195], v[32:33], off
	s_waitcnt vmcnt(21)
	v_mfma_f32_32x32x16_bf16 v[0:15], v[104:107], v[100:103], 0
	v_mfma_f32_32x32x16_bf16 v[0:15], v[108:111], v[100:103], v[0:15]
	global_load_dwordx4 v[100:103], v[56:57], off
	global_load_dwordx4 v[104:107], v[16:17], off offset:256
	global_load_dwordx4 v[108:111], v[34:35], off
	s_waitcnt vmcnt(21)
	v_mfma_f32_32x32x16_bf16 v[0:15], v[116:119], v[112:115], v[0:15]
	v_mfma_f32_32x32x16_bf16 v[0:15], v[120:123], v[112:115], v[0:15]
	global_load_dwordx4 v[112:115], v[56:57], off offset:32
	global_load_dwordx4 v[116:119], v[16:17], off offset:288
	global_load_dwordx4 v[120:123], v[36:37], off
	s_waitcnt vmcnt(21)
	v_mfma_f32_32x32x16_bf16 v[0:15], v[128:131], v[124:127], v[0:15]
	v_mfma_f32_32x32x16_bf16 v[0:15], v[132:135], v[124:127], v[0:15]
	global_load_dwordx4 v[124:127], v[56:57], off offset:64
	global_load_dwordx4 v[128:131], v[16:17], off offset:320
	global_load_dwordx4 v[132:135], v[38:39], off
	s_waitcnt vmcnt(21)
	v_mfma_f32_32x32x16_bf16 v[0:15], v[140:143], v[136:139], v[0:15]
	v_mfma_f32_32x32x16_bf16 v[0:15], v[144:147], v[136:139], v[0:15]
	global_load_dwordx4 v[136:139], v[56:57], off offset:96
	global_load_dwordx4 v[140:143], v[16:17], off offset:352
	global_load_dwordx4 v[144:147], v[40:41], off
	s_waitcnt vmcnt(21)
	v_mfma_f32_32x32x16_bf16 v[0:15], v[152:155], v[148:151], v[0:15]
	v_mfma_f32_32x32x16_bf16 v[0:15], v[156:159], v[148:151], v[0:15]
	global_load_dwordx4 v[148:151], v[56:57], off offset:128
	global_load_dwordx4 v[152:155], v[16:17], off offset:384
	global_load_dwordx4 v[156:159], v[42:43], off
	s_waitcnt vmcnt(21)
	v_mfma_f32_32x32x16_bf16 v[0:15], v[164:167], v[160:163], v[0:15]
	v_mfma_f32_32x32x16_bf16 v[0:15], v[168:171], v[160:163], v[0:15]
	global_load_dwordx4 v[160:163], v[56:57], off offset:160
	global_load_dwordx4 v[164:167], v[16:17], off offset:416
	global_load_dwordx4 v[168:171], v[44:45], off
	s_waitcnt vmcnt(21)
	v_mfma_f32_32x32x16_bf16 v[0:15], v[176:179], v[172:175], v[0:15]
	v_mfma_f32_32x32x16_bf16 v[0:15], v[180:183], v[172:175], v[0:15]
	global_load_dwordx4 v[172:175], v[56:57], off offset:192
	global_load_dwordx4 v[176:179], v[16:17], off offset:448
	global_load_dwordx4 v[180:183], v[46:47], off
	s_waitcnt vmcnt(21)
	v_mfma_f32_32x32x16_bf16 v[0:15], v[188:191], v[184:187], v[0:15]
	v_mfma_f32_32x32x16_bf16 v[0:15], v[192:195], v[184:187], v[0:15]
	global_load_dwordx4 v[184:187], v[56:57], off offset:224
	global_load_dwordx4 v[188:191], v[16:17], off offset:480
	global_load_dwordx4 v[192:195], v[48:49], off
	s_waitcnt vmcnt(21)
	v_mfma_f32_32x32x16_bf16 v[0:15], v[104:107], v[100:103], v[0:15]
	v_mfma_f32_32x32x16_bf16 v[0:15], v[108:111], v[100:103], v[0:15]
	s_waitcnt vmcnt(18)
	v_mfma_f32_32x32x16_bf16 v[0:15], v[116:119], v[112:115], v[0:15]
	v_mfma_f32_32x32x16_bf16 v[0:15], v[120:123], v[112:115], v[0:15]
	s_waitcnt vmcnt(15)
	v_mfma_f32_32x32x16_bf16 v[0:15], v[128:131], v[124:127], v[0:15]
	v_mfma_f32_32x32x16_bf16 v[0:15], v[132:135], v[124:127], v[0:15]
	s_waitcnt vmcnt(12)
	v_mfma_f32_32x32x16_bf16 v[0:15], v[140:143], v[136:139], v[0:15]
	v_mfma_f32_32x32x16_bf16 v[0:15], v[144:147], v[136:139], v[0:15]
	s_waitcnt vmcnt(9)
	v_mfma_f32_32x32x16_bf16 v[0:15], v[152:155], v[148:151], v[0:15]
	v_mfma_f32_32x32x16_bf16 v[0:15], v[156:159], v[148:151], v[0:15]
	s_waitcnt vmcnt(6)
	v_mfma_f32_32x32x16_bf16 v[0:15], v[164:167], v[160:163], v[0:15]
	v_mfma_f32_32x32x16_bf16 v[0:15], v[168:171], v[160:163], v[0:15]
	s_waitcnt vmcnt(3)
	v_mfma_f32_32x32x16_bf16 v[0:15], v[176:179], v[172:175], v[0:15]
	v_mfma_f32_32x32x16_bf16 v[0:15], v[180:183], v[172:175], v[0:15]
	s_waitcnt vmcnt(0)
	v_mfma_f32_32x32x16_bf16 v[0:15], v[188:191], v[184:187], v[0:15]
	v_mfma_f32_32x32x16_bf16 v[0:15], v[192:195], v[184:187], v[0:15]
	s_nop 11
	ds_write_b128 v88, v[0:3]
	ds_write_b128 v88, v[4:7] offset:32
	ds_write_b128 v88, v[8:11] offset:64
	ds_write_b128 v88, v[12:15] offset:96
	s_waitcnt lgkmcnt(0)
	s_barrier
	s_and_saveexec_b64 s[84:85], s[4:5]
	s_cbranch_execz .LBB0_1347
	global_load_dwordx4 v[0:3], v97, s[24:25] offset:48
	global_load_dwordx4 v[4:7], v97, s[24:25] offset:32
	global_load_dwordx4 v[8:11], v97, s[24:25] offset:16
	global_load_dwordx4 v[12:15], v97, s[24:25]
	ds_read_b128 v[58:61], v89
	ds_read_b128 v[62:65], v89 offset:16
	ds_read_b128 v[70:73], v89 offset:32
	ds_read_b128 v[90:93], v89 offset:48
	s_mov_b32 s8, 0xff800000
	s_waitcnt vmcnt(0) lgkmcnt(3)
	v_pk_add_f32 v[60:61], v[14:15], v[60:61]
	v_pk_add_f32 v[58:59], v[12:13], v[58:59]
	ds_read_b128 v[12:15], v89 offset:9216
	s_waitcnt lgkmcnt(0)
	v_pk_add_f32 v[60:61], v[60:61], v[14:15]
	v_pk_add_f32 v[58:59], v[58:59], v[12:13]
	ds_read_b128 v[12:15], v89 offset:18432
	s_waitcnt lgkmcnt(0)
	v_pk_add_f32 v[60:61], v[60:61], v[14:15]
	v_pk_add_f32 v[58:59], v[58:59], v[12:13]
	ds_read_b128 v[12:15], v89 offset:27648
	s_waitcnt lgkmcnt(0)
	v_pk_add_f32 v[66:67], v[60:61], v[14:15]
	v_pk_add_f32 v[68:69], v[58:59], v[12:13]
	v_pk_add_f32 v[12:13], v[10:11], v[64:65]
	v_pk_add_f32 v[14:15], v[8:9], v[62:63]
	ds_read_b128 v[8:11], v89 offset:9232
	v_cmp_lg_f32_e32 vcc, s8, v68
	v_cmp_nlg_f32_e64 s[8:9], s8, v68
	s_waitcnt lgkmcnt(0)
	v_pk_add_f32 v[12:13], v[12:13], v[10:11]
	v_pk_add_f32 v[14:15], v[14:15], v[8:9]
	ds_read_b128 v[8:11], v89 offset:18448
	v_cndmask_b32_e32 v55, v242, v68, vcc
	v_cmp_gt_f32_e32 vcc, v69, v55
	s_waitcnt lgkmcnt(0)
	v_pk_add_f32 v[12:13], v[12:13], v[10:11]
	v_pk_add_f32 v[14:15], v[14:15], v[8:9]
	ds_read_b128 v[8:11], v89 offset:27664
	v_cndmask_b32_e32 v55, v55, v69, vcc
	s_waitcnt lgkmcnt(0)
	v_pk_add_f32 v[62:63], v[12:13], v[10:11]
	v_pk_add_f32 v[64:65], v[14:15], v[8:9]
	v_pk_add_f32 v[8:9], v[6:7], v[72:73]
	v_pk_add_f32 v[10:11], v[4:5], v[70:71]
	ds_read_b128 v[4:7], v89 offset:9248
	s_waitcnt lgkmcnt(0)
	v_pk_add_f32 v[8:9], v[8:9], v[6:7]
	v_pk_add_f32 v[10:11], v[10:11], v[4:5]
	ds_read_b128 v[4:7], v89 offset:18464
	s_waitcnt lgkmcnt(0)
	v_pk_add_f32 v[8:9], v[8:9], v[6:7]
	v_pk_add_f32 v[10:11], v[10:11], v[4:5]
	ds_read_b128 v[4:7], v89 offset:27680
	s_waitcnt lgkmcnt(0)
	v_pk_add_f32 v[58:59], v[8:9], v[6:7]
	v_pk_add_f32 v[60:61], v[10:11], v[4:5]
	v_pk_add_f32 v[4:5], v[2:3], v[92:93]
	v_pk_add_f32 v[6:7], v[0:1], v[90:91]
	ds_read_b128 v[0:3], v89 offset:9264
	s_waitcnt lgkmcnt(0)
	v_pk_add_f32 v[4:5], v[4:5], v[2:3]
	v_pk_add_f32 v[6:7], v[6:7], v[0:1]
	ds_read_b128 v[0:3], v89 offset:18480
	s_waitcnt lgkmcnt(0)
	v_pk_add_f32 v[4:5], v[4:5], v[2:3]
	v_pk_add_f32 v[6:7], v[6:7], v[0:1]
	ds_read_b128 v[0:3], v89 offset:27696
	s_waitcnt lgkmcnt(0)
	v_pk_add_f32 v[12:13], v[4:5], v[2:3]
	v_pk_add_f32 v[14:15], v[6:7], v[0:1]
	global_load_dwordx4 v[0:3], v97, s[24:25] offset:112
	global_load_dwordx4 v[4:7], v97, s[24:25] offset:96
	global_load_dwordx4 v[8:11], v97, s[24:25] offset:80
	global_load_dwordx4 v[70:73], v97, s[24:25] offset:64
	ds_read_b128 v[90:93], v89 offset:64
	s_waitcnt vmcnt(0) lgkmcnt(0)
	v_pk_add_f32 v[92:93], v[72:73], v[92:93]
	v_pk_add_f32 v[90:91], v[70:71], v[90:91]
	ds_read_b128 v[70:73], v89 offset:9280
	s_waitcnt lgkmcnt(0)
	v_pk_add_f32 v[92:93], v[92:93], v[72:73]
	v_pk_add_f32 v[90:91], v[90:91], v[70:71]
	ds_read_b128 v[70:73], v89 offset:18496
	s_waitcnt lgkmcnt(0)
	v_pk_add_f32 v[72:73], v[92:93], v[72:73]
	v_pk_add_f32 v[94:95], v[90:91], v[70:71]
	ds_read_b128 v[90:93], v89 offset:27712
	s_waitcnt lgkmcnt(0)
	v_pk_add_f32 v[70:71], v[72:73], v[92:93]
	v_pk_add_f32 v[72:73], v[94:95], v[90:91]
	ds_read_b128 v[90:93], v89 offset:80
	s_waitcnt lgkmcnt(0)
	v_pk_add_f32 v[92:93], v[10:11], v[92:93]
	v_pk_add_f32 v[90:91], v[8:9], v[90:91]
	ds_read_b128 v[8:11], v89 offset:9296
	s_waitcnt lgkmcnt(0)
	v_pk_add_f32 v[92:93], v[92:93], v[10:11]
	v_pk_add_f32 v[90:91], v[90:91], v[8:9]
	ds_read_b128 v[8:11], v89 offset:18512
	s_waitcnt lgkmcnt(0)
	v_pk_add_f32 v[10:11], v[92:93], v[10:11]
	v_pk_add_f32 v[94:95], v[90:91], v[8:9]
	ds_read_b128 v[90:93], v89 offset:27728
	s_waitcnt lgkmcnt(0)
	v_pk_add_f32 v[8:9], v[10:11], v[92:93]
	v_pk_add_f32 v[10:11], v[94:95], v[90:91]
	ds_read_b128 v[90:93], v89 offset:96
	s_waitcnt lgkmcnt(0)
	v_pk_add_f32 v[92:93], v[6:7], v[92:93]
	v_pk_add_f32 v[90:91], v[4:5], v[90:91]
	ds_read_b128 v[4:7], v89 offset:9312
	s_waitcnt lgkmcnt(0)
	v_pk_add_f32 v[92:93], v[92:93], v[6:7]
	v_pk_add_f32 v[90:91], v[90:91], v[4:5]
	ds_read_b128 v[4:7], v89 offset:18528
	s_waitcnt lgkmcnt(0)
	v_pk_add_f32 v[6:7], v[92:93], v[6:7]
	v_pk_add_f32 v[94:95], v[90:91], v[4:5]
	ds_read_b128 v[90:93], v89 offset:27744
	s_waitcnt lgkmcnt(0)
	v_pk_add_f32 v[4:5], v[6:7], v[92:93]
	v_pk_add_f32 v[6:7], v[94:95], v[90:91]
	ds_read_b128 v[90:93], v89 offset:112
	s_waitcnt lgkmcnt(0)
	v_pk_add_f32 v[92:93], v[2:3], v[92:93]
	v_pk_add_f32 v[90:91], v[0:1], v[90:91]
	ds_read_b128 v[0:3], v89 offset:9328
	s_waitcnt lgkmcnt(0)
	v_pk_add_f32 v[92:93], v[92:93], v[2:3]
	v_pk_add_f32 v[90:91], v[90:91], v[0:1]
	ds_read_b128 v[0:3], v89 offset:18544
	s_waitcnt lgkmcnt(0)
	v_pk_add_f32 v[2:3], v[92:93], v[2:3]
	v_pk_add_f32 v[94:95], v[90:91], v[0:1]
	ds_read_b128 v[90:93], v89 offset:27760
	s_waitcnt lgkmcnt(0)
	v_pk_add_f32 v[0:1], v[2:3], v[92:93]
	v_pk_add_f32 v[2:3], v[94:95], v[90:91]
	v_cndmask_b32_e64 v90, 0, 1, vcc
	v_cmp_gt_f32_e32 vcc, v66, v55
	s_nop 1
	v_cndmask_b32_e32 v55, v55, v66, vcc
	v_cndmask_b32_e64 v90, v90, 2, vcc
	v_cmp_gt_f32_e32 vcc, v67, v55
	s_nop 1
	v_cndmask_b32_e32 v55, v55, v67, vcc
	v_cndmask_b32_e64 v90, v90, 3, vcc
	v_cmp_gt_f32_e32 vcc, v64, v55
	s_nop 1
	v_cndmask_b32_e32 v55, v55, v64, vcc
	v_cndmask_b32_e64 v90, v90, 4, vcc
	v_cmp_gt_f32_e32 vcc, v65, v55
	s_nop 1
	v_cndmask_b32_e32 v55, v55, v65, vcc
	v_cndmask_b32_e64 v90, v90, 5, vcc
	v_cmp_gt_f32_e32 vcc, v62, v55
	s_nop 1
	v_cndmask_b32_e32 v55, v55, v62, vcc
	v_cndmask_b32_e64 v90, v90, 6, vcc
	v_cmp_gt_f32_e32 vcc, v63, v55
	s_nop 1
	v_cndmask_b32_e32 v55, v55, v63, vcc
	v_cndmask_b32_e64 v90, v90, 7, vcc
	v_cmp_gt_f32_e32 vcc, v60, v55
	s_nop 1
	v_cndmask_b32_e32 v55, v55, v60, vcc
	v_cndmask_b32_e64 v90, v90, 8, vcc
	v_cmp_gt_f32_e32 vcc, v61, v55
	s_nop 1
	v_cndmask_b32_e32 v55, v55, v61, vcc
	v_cndmask_b32_e64 v90, v90, 9, vcc
	v_cmp_gt_f32_e32 vcc, v58, v55
	s_nop 1
	v_cndmask_b32_e32 v55, v55, v58, vcc
	v_cndmask_b32_e64 v90, v90, 10, vcc
	v_cmp_gt_f32_e32 vcc, v59, v55
	s_nop 1
	v_cndmask_b32_e32 v55, v55, v59, vcc
	v_cndmask_b32_e64 v90, v90, 11, vcc
	v_cmp_gt_f32_e32 vcc, v14, v55
	s_nop 1
	v_cndmask_b32_e32 v55, v55, v14, vcc
	v_cndmask_b32_e64 v90, v90, 12, vcc
	v_cmp_gt_f32_e32 vcc, v15, v55
	s_nop 1
	v_cndmask_b32_e32 v55, v55, v15, vcc
	v_cndmask_b32_e64 v90, v90, 13, vcc
	v_cmp_gt_f32_e32 vcc, v12, v55
	s_nop 1
	v_cndmask_b32_e32 v55, v55, v12, vcc
	v_cndmask_b32_e64 v90, v90, 14, vcc
	v_cmp_gt_f32_e32 vcc, v13, v55
	s_nop 1
	v_cndmask_b32_e32 v55, v55, v13, vcc
	v_cndmask_b32_e64 v90, v90, 15, vcc
	v_cmp_gt_f32_e32 vcc, v72, v55
	s_nop 1
	v_cndmask_b32_e32 v55, v55, v72, vcc
	v_cndmask_b32_e64 v90, v90, 16, vcc
	v_cmp_gt_f32_e32 vcc, v73, v55
	s_nop 1
	v_cndmask_b32_e32 v55, v55, v73, vcc
	v_cndmask_b32_e64 v90, v90, 17, vcc
	v_cmp_gt_f32_e32 vcc, v70, v55
	s_nop 1
	v_cndmask_b32_e32 v55, v55, v70, vcc
	v_cndmask_b32_e64 v90, v90, 18, vcc
	v_cmp_gt_f32_e32 vcc, v71, v55
	s_nop 1
	v_cndmask_b32_e32 v55, v55, v71, vcc
	v_cndmask_b32_e64 v90, v90, 19, vcc
	v_cmp_gt_f32_e32 vcc, v10, v55
	s_nop 1
	v_cndmask_b32_e32 v55, v55, v10, vcc
	v_cndmask_b32_e64 v90, v90, 20, vcc
	v_cmp_gt_f32_e32 vcc, v11, v55
	s_nop 1
	v_cndmask_b32_e32 v55, v55, v11, vcc
	v_cndmask_b32_e64 v90, v90, 21, vcc
	v_cmp_gt_f32_e32 vcc, v8, v55
	s_nop 1
	v_cndmask_b32_e32 v55, v55, v8, vcc
	v_cndmask_b32_e64 v90, v90, 22, vcc
	v_cmp_gt_f32_e32 vcc, v9, v55
	s_nop 1
	v_cndmask_b32_e32 v55, v55, v9, vcc
	v_cndmask_b32_e64 v90, v90, 23, vcc
	v_cmp_gt_f32_e32 vcc, v6, v55
	s_nop 1
	v_cndmask_b32_e32 v55, v55, v6, vcc
	v_cndmask_b32_e64 v90, v90, 24, vcc
	v_cmp_gt_f32_e32 vcc, v7, v55
	s_nop 1
	v_cndmask_b32_e32 v55, v55, v7, vcc
	v_cndmask_b32_e64 v90, v90, 25, vcc
	v_cmp_gt_f32_e32 vcc, v4, v55
	s_nop 1
	v_cndmask_b32_e32 v55, v55, v4, vcc
	v_cndmask_b32_e64 v90, v90, 26, vcc
	v_cmp_gt_f32_e32 vcc, v5, v55
	s_nop 1
	v_cndmask_b32_e32 v55, v55, v5, vcc
	v_cndmask_b32_e64 v90, v90, 27, vcc
	v_cmp_gt_f32_e32 vcc, v2, v55
	s_nop 1
	v_cndmask_b32_e32 v55, v55, v2, vcc
	v_cndmask_b32_e64 v90, v90, 28, vcc
	v_cmp_gt_f32_e32 vcc, v3, v55
	s_nop 1
	v_cndmask_b32_e32 v55, v55, v3, vcc
	v_cndmask_b32_e64 v90, v90, 29, vcc
	v_cmp_gt_f32_e32 vcc, v0, v55
	s_nop 1
	v_cndmask_b32_e32 v91, v55, v0, vcc
	v_cndmask_b32_e64 v90, v90, 30, vcc
	v_cmp_gt_f32_e32 vcc, v1, v91
	s_nop 1
	v_cndmask_b32_e64 v55, v90, 31, vcc
	v_cndmask_b32_e32 v90, v91, v1, vcc
	v_cmp_eq_u32_e32 vcc, 0, v55
	s_or_b64 s[8:9], vcc, s[8:9]
	v_cndmask_b32_e64 v91, v68, v242, s[8:9]
	v_cmp_eq_u32_e64 s[82:83], 1, v55
	v_cmp_ngt_f32_e32 vcc, v69, v91
	s_or_b64 vcc, s[82:83], vcc
	s_xor_b64 s[10:11], vcc, -1
	v_cndmask_b32_e32 v91, v69, v91, vcc
	v_cmp_eq_u32_e64 s[80:81], 2, v55
	v_cmp_ngt_f32_e32 vcc, v66, v91
	s_or_b64 vcc, s[80:81], vcc
	v_cndmask_b32_e64 v92, 0, 1, s[10:11]
	v_cndmask_b32_e32 v91, v66, v91, vcc
	v_cndmask_b32_e32 v92, 2, v92, vcc
	v_cmp_eq_u32_e64 s[78:79], 3, v55
	v_cmp_ngt_f32_e32 vcc, v67, v91
	s_or_b64 vcc, s[78:79], vcc
	v_cmp_eq_u32_e64 s[76:77], 4, v55
	v_cndmask_b32_e32 v91, v67, v91, vcc
	v_cndmask_b32_e32 v92, 3, v92, vcc
	v_cmp_ngt_f32_e32 vcc, v64, v91
	s_or_b64 vcc, s[76:77], vcc
	v_cmp_eq_u32_e64 s[74:75], 5, v55
	v_cndmask_b32_e32 v91, v64, v91, vcc
	v_cndmask_b32_e32 v92, 4, v92, vcc
	v_cmp_ngt_f32_e32 vcc, v65, v91
	s_or_b64 vcc, s[74:75], vcc
	v_cmp_eq_u32_e64 s[72:73], 6, v55
	v_cndmask_b32_e32 v91, v65, v91, vcc
	v_cndmask_b32_e32 v92, 5, v92, vcc
	v_cmp_ngt_f32_e32 vcc, v62, v91
	s_or_b64 vcc, s[72:73], vcc
	v_cmp_eq_u32_e64 s[70:71], 7, v55
	v_cndmask_b32_e32 v91, v62, v91, vcc
	v_cndmask_b32_e32 v92, 6, v92, vcc
	v_cmp_ngt_f32_e32 vcc, v63, v91
	s_or_b64 vcc, s[70:71], vcc
	v_cmp_eq_u32_e64 s[68:69], 8, v55
	v_cndmask_b32_e32 v91, v63, v91, vcc
	v_cndmask_b32_e32 v92, 7, v92, vcc
	v_cmp_ngt_f32_e32 vcc, v60, v91
	s_or_b64 vcc, s[68:69], vcc
	v_cmp_eq_u32_e64 s[66:67], 9, v55
	v_cndmask_b32_e32 v91, v60, v91, vcc
	v_cndmask_b32_e32 v92, 8, v92, vcc
	v_cmp_ngt_f32_e32 vcc, v61, v91
	s_or_b64 vcc, s[66:67], vcc
	v_cmp_eq_u32_e64 s[64:65], 10, v55
	v_cndmask_b32_e32 v91, v61, v91, vcc
	v_cndmask_b32_e32 v92, 9, v92, vcc
	v_cmp_ngt_f32_e32 vcc, v58, v91
	s_or_b64 vcc, s[64:65], vcc
	v_cmp_eq_u32_e64 s[62:63], 11, v55
	v_cndmask_b32_e32 v91, v58, v91, vcc
	v_cndmask_b32_e32 v92, 10, v92, vcc
	v_cmp_ngt_f32_e32 vcc, v59, v91
	s_or_b64 vcc, s[62:63], vcc
	v_cmp_eq_u32_e64 s[60:61], 12, v55
	v_cndmask_b32_e32 v91, v59, v91, vcc
	v_cndmask_b32_e32 v92, 11, v92, vcc
	v_cmp_ngt_f32_e32 vcc, v14, v91
	s_or_b64 vcc, s[60:61], vcc
	v_cmp_eq_u32_e64 s[58:59], 13, v55
	v_cndmask_b32_e32 v91, v14, v91, vcc
	v_cndmask_b32_e32 v92, 12, v92, vcc
	v_cmp_ngt_f32_e32 vcc, v15, v91
	s_or_b64 vcc, s[58:59], vcc
	v_cmp_eq_u32_e64 s[56:57], 14, v55
	v_cndmask_b32_e32 v91, v15, v91, vcc
	v_cndmask_b32_e32 v92, 13, v92, vcc
	v_cmp_ngt_f32_e32 vcc, v12, v91
	s_or_b64 vcc, s[56:57], vcc
	v_cmp_eq_u32_e64 s[54:55], 15, v55
	v_cndmask_b32_e32 v91, v12, v91, vcc
	v_cndmask_b32_e32 v92, 14, v92, vcc
	v_cmp_ngt_f32_e32 vcc, v13, v91
	s_or_b64 vcc, s[54:55], vcc
	v_cmp_eq_u32_e64 s[52:53], 16, v55
	v_cndmask_b32_e32 v91, v13, v91, vcc
	v_cndmask_b32_e32 v92, 15, v92, vcc
	v_cmp_ngt_f32_e32 vcc, v72, v91
	s_or_b64 vcc, s[52:53], vcc
	v_cmp_eq_u32_e64 s[50:51], 17, v55
	v_cndmask_b32_e32 v91, v72, v91, vcc
	v_cndmask_b32_e32 v92, 16, v92, vcc
	v_cmp_ngt_f32_e32 vcc, v73, v91
	s_or_b64 vcc, s[50:51], vcc
	v_cmp_eq_u32_e64 s[48:49], 18, v55
	v_cndmask_b32_e32 v91, v73, v91, vcc
	v_cndmask_b32_e32 v92, 17, v92, vcc
	v_cmp_ngt_f32_e32 vcc, v70, v91
	s_or_b64 vcc, s[48:49], vcc
	v_cmp_eq_u32_e64 s[46:47], 19, v55
	v_cndmask_b32_e32 v91, v70, v91, vcc
	v_cndmask_b32_e32 v92, 18, v92, vcc
	v_cmp_ngt_f32_e32 vcc, v71, v91
	s_or_b64 vcc, s[46:47], vcc
	v_cmp_eq_u32_e64 s[44:45], 20, v55
	v_cndmask_b32_e32 v91, v71, v91, vcc
	v_cndmask_b32_e32 v92, 19, v92, vcc
	v_cmp_ngt_f32_e32 vcc, v10, v91
	s_or_b64 vcc, s[44:45], vcc
	v_cmp_eq_u32_e64 s[42:43], 21, v55
	v_cndmask_b32_e32 v91, v10, v91, vcc
	v_cndmask_b32_e32 v92, 20, v92, vcc
	v_cmp_ngt_f32_e32 vcc, v11, v91
	s_or_b64 vcc, s[42:43], vcc
	v_cmp_eq_u32_e64 s[40:41], 22, v55
	v_cndmask_b32_e32 v91, v11, v91, vcc
	v_cndmask_b32_e32 v92, 21, v92, vcc
	v_cmp_ngt_f32_e32 vcc, v8, v91
	s_or_b64 vcc, s[40:41], vcc
	v_cmp_eq_u32_e64 s[38:39], 23, v55
	v_cndmask_b32_e32 v91, v8, v91, vcc
	v_cndmask_b32_e32 v92, 22, v92, vcc
	v_cmp_ngt_f32_e32 vcc, v9, v91
	s_or_b64 vcc, s[38:39], vcc
	v_cmp_eq_u32_e64 s[36:37], 24, v55
	v_cndmask_b32_e32 v91, v9, v91, vcc
	v_cndmask_b32_e32 v92, 23, v92, vcc
	v_cmp_ngt_f32_e32 vcc, v6, v91
	s_or_b64 vcc, s[36:37], vcc
	v_cmp_eq_u32_e64 s[20:21], 25, v55
	v_cndmask_b32_e32 v91, v6, v91, vcc
	v_cndmask_b32_e32 v92, 24, v92, vcc
	v_cmp_ngt_f32_e32 vcc, v7, v91
	s_or_b64 vcc, s[20:21], vcc
	v_cmp_eq_u32_e64 s[18:19], 26, v55
	v_cndmask_b32_e32 v91, v7, v91, vcc
	v_cndmask_b32_e32 v92, 25, v92, vcc
	v_cmp_ngt_f32_e32 vcc, v4, v91
	s_or_b64 vcc, s[18:19], vcc
	v_cmp_eq_u32_e64 s[16:17], 27, v55
	v_cndmask_b32_e32 v91, v4, v91, vcc
	v_cndmask_b32_e32 v92, 26, v92, vcc
	v_cmp_ngt_f32_e32 vcc, v5, v91
	s_or_b64 vcc, s[16:17], vcc
	v_cmp_eq_u32_e64 s[14:15], 28, v55
	v_cndmask_b32_e32 v91, v5, v91, vcc
	v_cndmask_b32_e32 v92, 27, v92, vcc
	v_cmp_ngt_f32_e32 vcc, v2, v91
	s_or_b64 vcc, s[14:15], vcc
	v_cmp_eq_u32_e64 s[12:13], 29, v55
	v_cndmask_b32_e32 v91, v2, v91, vcc
	v_cndmask_b32_e32 v92, 28, v92, vcc
	v_cmp_ngt_f32_e32 vcc, v3, v91
	s_or_b64 vcc, s[12:13], vcc
	v_cmp_eq_u32_e64 s[10:11], 30, v55
	v_cndmask_b32_e32 v91, v3, v91, vcc
	v_cndmask_b32_e32 v92, 29, v92, vcc
	v_cmp_ngt_f32_e32 vcc, v0, v91
	s_or_b64 vcc, s[10:11], vcc
	s_nop 0
	v_cndmask_b32_e32 v93, v0, v91, vcc
	v_cndmask_b32_e32 v92, 30, v92, vcc
	v_cmp_eq_u32_e32 vcc, 31, v55
	v_cmp_ngt_f32_e64 s[22:23], v1, v93
	s_or_b64 s[22:23], vcc, s[22:23]
	s_nop 0
	v_cndmask_b32_e64 v91, 31, v92, s[22:23]
	v_cndmask_b32_e64 v92, v1, v93, s[22:23]
	v_cmp_eq_u32_e64 s[22:23], 0, v91
	s_or_b64 s[8:9], s[8:9], s[22:23]
	v_cndmask_b32_e64 v93, v68, v242, s[8:9]
	v_cmp_eq_u32_e64 s[22:23], 1, v91
	s_or_b64 s[82:83], s[82:83], s[22:23]
	v_cmp_ngt_f32_e64 s[22:23], v69, v93
	s_or_b64 s[22:23], s[82:83], s[22:23]
	s_xor_b64 s[88:89], s[22:23], -1
	v_cndmask_b32_e64 v93, v69, v93, s[22:23]
	v_cmp_eq_u32_e64 s[22:23], 2, v91
	s_or_b64 s[80:81], s[80:81], s[22:23]
	v_cmp_ngt_f32_e64 s[22:23], v66, v93
	v_cndmask_b32_e64 v94, 0, 1, s[88:89]
	s_or_b64 s[22:23], s[80:81], s[22:23]
	v_cndmask_b32_e64 v94, 2, v94, s[22:23]
	v_cndmask_b32_e64 v93, v66, v93, s[22:23]
	v_cmp_eq_u32_e64 s[22:23], 3, v91
	s_or_b64 s[78:79], s[78:79], s[22:23]
	v_cmp_ngt_f32_e64 s[22:23], v67, v93
	s_or_b64 s[22:23], s[78:79], s[22:23]
	v_readlane_b32 s88, v252, 6
	v_cndmask_b32_e64 v94, 3, v94, s[22:23]
	v_cndmask_b32_e64 v93, v67, v93, s[22:23]
	v_cmp_eq_u32_e64 s[22:23], 4, v91
	s_or_b64 s[76:77], s[76:77], s[22:23]
	v_cmp_ngt_f32_e64 s[22:23], v64, v93
	s_or_b64 s[22:23], s[76:77], s[22:23]
	v_readlane_b32 s89, v252, 7
	v_cndmask_b32_e64 v94, 4, v94, s[22:23]
	v_cndmask_b32_e64 v93, v64, v93, s[22:23]
	v_cmp_eq_u32_e64 s[22:23], 5, v91
	s_or_b64 s[74:75], s[74:75], s[22:23]
	v_cmp_ngt_f32_e64 s[22:23], v65, v93
	s_or_b64 s[22:23], s[74:75], s[22:23]
	s_nop 0
	v_cndmask_b32_e64 v94, 5, v94, s[22:23]
	v_cndmask_b32_e64 v93, v65, v93, s[22:23]
	v_cmp_eq_u32_e64 s[22:23], 6, v91
	s_or_b64 s[72:73], s[72:73], s[22:23]
	v_cmp_ngt_f32_e64 s[22:23], v62, v93
	s_or_b64 s[22:23], s[72:73], s[22:23]
	s_nop 0
	v_cndmask_b32_e64 v94, 6, v94, s[22:23]
	v_cndmask_b32_e64 v93, v62, v93, s[22:23]
	v_cmp_eq_u32_e64 s[22:23], 7, v91
	s_or_b64 s[70:71], s[70:71], s[22:23]
	v_cmp_ngt_f32_e64 s[22:23], v63, v93
	s_or_b64 s[22:23], s[70:71], s[22:23]
	s_nop 0
	v_cndmask_b32_e64 v94, 7, v94, s[22:23]
	v_cndmask_b32_e64 v93, v63, v93, s[22:23]
	v_cmp_eq_u32_e64 s[22:23], 8, v91
	s_or_b64 s[68:69], s[68:69], s[22:23]
	v_cmp_ngt_f32_e64 s[22:23], v60, v93
	s_or_b64 s[22:23], s[68:69], s[22:23]
	s_nop 0
	v_cndmask_b32_e64 v94, 8, v94, s[22:23]
	v_cndmask_b32_e64 v93, v60, v93, s[22:23]
	v_cmp_eq_u32_e64 s[22:23], 9, v91
	s_or_b64 s[66:67], s[66:67], s[22:23]
	v_cmp_ngt_f32_e64 s[22:23], v61, v93
	s_or_b64 s[22:23], s[66:67], s[22:23]
	s_nop 0
	v_cndmask_b32_e64 v94, 9, v94, s[22:23]
	v_cndmask_b32_e64 v93, v61, v93, s[22:23]
	v_cmp_eq_u32_e64 s[22:23], 10, v91
	s_or_b64 s[64:65], s[64:65], s[22:23]
	v_cmp_ngt_f32_e64 s[22:23], v58, v93
	s_or_b64 s[22:23], s[64:65], s[22:23]
	s_nop 0
	v_cndmask_b32_e64 v94, 10, v94, s[22:23]
	v_cndmask_b32_e64 v93, v58, v93, s[22:23]
	v_cmp_eq_u32_e64 s[22:23], 11, v91
	s_or_b64 s[62:63], s[62:63], s[22:23]
	v_cmp_ngt_f32_e64 s[22:23], v59, v93
	s_or_b64 s[22:23], s[62:63], s[22:23]
	s_nop 0
	v_cndmask_b32_e64 v94, 11, v94, s[22:23]
	v_cndmask_b32_e64 v93, v59, v93, s[22:23]
	v_cmp_eq_u32_e64 s[22:23], 12, v91
	s_or_b64 s[60:61], s[60:61], s[22:23]
	v_cmp_ngt_f32_e64 s[22:23], v14, v93
	s_or_b64 s[22:23], s[60:61], s[22:23]
	s_nop 0
	v_cndmask_b32_e64 v94, 12, v94, s[22:23]
	v_cndmask_b32_e64 v93, v14, v93, s[22:23]
	v_cmp_eq_u32_e64 s[22:23], 13, v91
	s_or_b64 s[58:59], s[58:59], s[22:23]
	v_cmp_ngt_f32_e64 s[22:23], v15, v93
	s_or_b64 s[22:23], s[58:59], s[22:23]
	s_nop 0
	v_cndmask_b32_e64 v94, 13, v94, s[22:23]
	v_cndmask_b32_e64 v93, v15, v93, s[22:23]
	v_cmp_eq_u32_e64 s[22:23], 14, v91
	s_or_b64 s[56:57], s[56:57], s[22:23]
	v_cmp_ngt_f32_e64 s[22:23], v12, v93
	s_or_b64 s[22:23], s[56:57], s[22:23]
	s_nop 0
	v_cndmask_b32_e64 v94, 14, v94, s[22:23]
	v_cndmask_b32_e64 v93, v12, v93, s[22:23]
	v_cmp_eq_u32_e64 s[22:23], 15, v91
	s_or_b64 s[54:55], s[54:55], s[22:23]
	v_cmp_ngt_f32_e64 s[22:23], v13, v93
	s_or_b64 s[22:23], s[54:55], s[22:23]
	s_nop 0
	v_cndmask_b32_e64 v94, 15, v94, s[22:23]
	v_cndmask_b32_e64 v93, v13, v93, s[22:23]
	v_cmp_eq_u32_e64 s[22:23], 16, v91
	s_or_b64 s[52:53], s[52:53], s[22:23]
	v_cmp_ngt_f32_e64 s[22:23], v72, v93
	s_or_b64 s[22:23], s[52:53], s[22:23]
	s_nop 0
	v_cndmask_b32_e64 v94, 16, v94, s[22:23]
	v_cndmask_b32_e64 v93, v72, v93, s[22:23]
	v_cmp_eq_u32_e64 s[22:23], 17, v91
	s_or_b64 s[50:51], s[50:51], s[22:23]
	v_cmp_ngt_f32_e64 s[22:23], v73, v93
	s_or_b64 s[22:23], s[50:51], s[22:23]
	s_nop 0
	v_cndmask_b32_e64 v94, 17, v94, s[22:23]
	v_cndmask_b32_e64 v93, v73, v93, s[22:23]
	v_cmp_eq_u32_e64 s[22:23], 18, v91
	s_or_b64 s[48:49], s[48:49], s[22:23]
	v_cmp_ngt_f32_e64 s[22:23], v70, v93
	s_or_b64 s[22:23], s[48:49], s[22:23]
	s_nop 0
	v_cndmask_b32_e64 v94, 18, v94, s[22:23]
	v_cndmask_b32_e64 v93, v70, v93, s[22:23]
	v_cmp_eq_u32_e64 s[22:23], 19, v91
	s_or_b64 s[46:47], s[46:47], s[22:23]
	v_cmp_ngt_f32_e64 s[22:23], v71, v93
	s_or_b64 s[22:23], s[46:47], s[22:23]
	s_nop 0
	v_cndmask_b32_e64 v94, 19, v94, s[22:23]
	v_cndmask_b32_e64 v93, v71, v93, s[22:23]
	v_cmp_eq_u32_e64 s[22:23], 20, v91
	s_or_b64 s[44:45], s[44:45], s[22:23]
	v_cmp_ngt_f32_e64 s[22:23], v10, v93
	s_or_b64 s[22:23], s[44:45], s[22:23]
	s_nop 0
	v_cndmask_b32_e64 v94, 20, v94, s[22:23]
	v_cndmask_b32_e64 v93, v10, v93, s[22:23]
	v_cmp_eq_u32_e64 s[22:23], 21, v91
	s_or_b64 s[42:43], s[42:43], s[22:23]
	v_cmp_ngt_f32_e64 s[22:23], v11, v93
	s_or_b64 s[22:23], s[42:43], s[22:23]
	s_nop 0
	v_cndmask_b32_e64 v94, 21, v94, s[22:23]
	v_cndmask_b32_e64 v93, v11, v93, s[22:23]
	v_cmp_eq_u32_e64 s[22:23], 22, v91
	s_or_b64 s[40:41], s[40:41], s[22:23]
	v_cmp_ngt_f32_e64 s[22:23], v8, v93
	s_or_b64 s[22:23], s[40:41], s[22:23]
	s_nop 0
	v_cndmask_b32_e64 v94, 22, v94, s[22:23]
	v_cndmask_b32_e64 v93, v8, v93, s[22:23]
	v_cmp_eq_u32_e64 s[22:23], 23, v91
	s_or_b64 s[38:39], s[38:39], s[22:23]
	v_cmp_ngt_f32_e64 s[22:23], v9, v93
	s_or_b64 s[22:23], s[38:39], s[22:23]
	s_nop 0
	v_cndmask_b32_e64 v94, 23, v94, s[22:23]
	v_cndmask_b32_e64 v93, v9, v93, s[22:23]
	v_cmp_eq_u32_e64 s[22:23], 24, v91
	s_or_b64 s[36:37], s[36:37], s[22:23]
	v_cmp_ngt_f32_e64 s[22:23], v6, v93
	s_or_b64 s[22:23], s[36:37], s[22:23]
	s_nop 0
	v_cndmask_b32_e64 v94, 24, v94, s[22:23]
	v_cndmask_b32_e64 v93, v6, v93, s[22:23]
	v_cmp_eq_u32_e64 s[22:23], 25, v91
	s_or_b64 s[22:23], s[20:21], s[22:23]
	v_cmp_ngt_f32_e64 s[20:21], v7, v93
	s_or_b64 s[20:21], s[22:23], s[20:21]
	s_nop 0
	v_cndmask_b32_e64 v94, 25, v94, s[20:21]
	v_cndmask_b32_e64 v93, v7, v93, s[20:21]
	v_cmp_eq_u32_e64 s[20:21], 26, v91
	s_or_b64 s[20:21], s[18:19], s[20:21]
	v_cmp_ngt_f32_e64 s[18:19], v4, v93
	s_or_b64 s[18:19], s[20:21], s[18:19]
	s_nop 0
	v_cndmask_b32_e64 v94, 26, v94, s[18:19]
	v_cndmask_b32_e64 v93, v4, v93, s[18:19]
	v_cmp_eq_u32_e64 s[18:19], 27, v91
	s_or_b64 s[18:19], s[16:17], s[18:19]
	v_cmp_ngt_f32_e64 s[16:17], v5, v93
	s_or_b64 s[16:17], s[18:19], s[16:17]
	s_nop 0
	v_cndmask_b32_e64 v94, 27, v94, s[16:17]
	v_cndmask_b32_e64 v93, v5, v93, s[16:17]
	v_cmp_eq_u32_e64 s[16:17], 28, v91
	s_or_b64 s[16:17], s[14:15], s[16:17]
	v_cmp_ngt_f32_e64 s[14:15], v2, v93
	s_or_b64 s[14:15], s[16:17], s[14:15]
	s_nop 0
	v_cndmask_b32_e64 v94, 28, v94, s[14:15]
	v_cndmask_b32_e64 v93, v2, v93, s[14:15]
	v_cmp_eq_u32_e64 s[14:15], 29, v91
	s_or_b64 s[14:15], s[12:13], s[14:15]
	v_cmp_ngt_f32_e64 s[12:13], v3, v93
	s_or_b64 s[12:13], s[14:15], s[12:13]
	s_nop 0
	v_cndmask_b32_e64 v94, 29, v94, s[12:13]
	v_cndmask_b32_e64 v93, v3, v93, s[12:13]
	v_cmp_eq_u32_e64 s[12:13], 30, v91
	s_or_b64 s[12:13], s[10:11], s[12:13]
	v_cmp_ngt_f32_e64 s[10:11], v0, v93
	s_or_b64 s[10:11], s[12:13], s[10:11]
	s_nop 0
	v_cndmask_b32_e64 v94, 30, v94, s[10:11]
	v_cndmask_b32_e64 v93, v0, v93, s[10:11]
	v_cmp_eq_u32_e64 s[10:11], 31, v91
	s_or_b64 s[10:11], vcc, s[10:11]
	v_cmp_ngt_f32_e32 vcc, v1, v93
	s_or_b64 vcc, s[10:11], vcc
	s_nop 0
	v_cndmask_b32_e32 v94, 31, v94, vcc
	v_cndmask_b32_e32 v93, v1, v93, vcc
	v_cmp_eq_u32_e32 vcc, 0, v94
	s_or_b64 vcc, s[8:9], vcc
	s_xor_b64 s[8:9], s[82:83], -1
	v_cndmask_b32_e32 v68, v68, v242, vcc
	v_cmp_ne_u32_e32 vcc, 1, v94
	s_and_b64 s[8:9], s[8:9], vcc
	v_cmp_gt_f32_e32 vcc, v69, v68
	s_and_b64 vcc, s[8:9], vcc
	s_xor_b64 s[8:9], s[80:81], -1
	v_cndmask_b32_e64 v95, 0, 1, vcc
	v_cndmask_b32_e32 v68, v68, v69, vcc
	v_cmp_ne_u32_e32 vcc, 2, v94
	s_and_b64 s[8:9], s[8:9], vcc
	v_cmp_gt_f32_e32 vcc, v66, v68
	s_and_b64 vcc, s[8:9], vcc
	s_xor_b64 s[8:9], s[78:79], -1
	v_cndmask_b32_e64 v69, v95, 2, vcc
	v_cndmask_b32_e32 v66, v68, v66, vcc
	v_cmp_ne_u32_e32 vcc, 3, v94
	s_and_b64 s[8:9], s[8:9], vcc
	v_cmp_gt_f32_e32 vcc, v67, v66
	s_and_b64 vcc, s[8:9], vcc
	s_xor_b64 s[8:9], s[76:77], -1
	v_cndmask_b32_e64 v68, v69, 3, vcc
	v_cndmask_b32_e32 v66, v66, v67, vcc
	v_cmp_ne_u32_e32 vcc, 4, v94
	s_and_b64 s[8:9], s[8:9], vcc
	v_cmp_gt_f32_e32 vcc, v64, v66
	s_and_b64 vcc, s[8:9], vcc
	s_xor_b64 s[8:9], s[74:75], -1
	v_cndmask_b32_e64 v67, v68, 4, vcc
	v_cndmask_b32_e32 v64, v66, v64, vcc
	v_cmp_ne_u32_e32 vcc, 5, v94
	s_and_b64 s[8:9], s[8:9], vcc
	v_cmp_gt_f32_e32 vcc, v65, v64
	s_and_b64 vcc, s[8:9], vcc
	s_xor_b64 s[8:9], s[72:73], -1
	v_cndmask_b32_e64 v66, v67, 5, vcc
	v_cndmask_b32_e32 v64, v64, v65, vcc
	v_cmp_ne_u32_e32 vcc, 6, v94
	s_and_b64 s[8:9], s[8:9], vcc
	v_cmp_gt_f32_e32 vcc, v62, v64
	s_and_b64 vcc, s[8:9], vcc
	s_xor_b64 s[8:9], s[70:71], -1
	v_cndmask_b32_e64 v65, v66, 6, vcc
	v_cndmask_b32_e32 v62, v64, v62, vcc
	v_cmp_ne_u32_e32 vcc, 7, v94
	s_and_b64 s[8:9], s[8:9], vcc
	v_cmp_gt_f32_e32 vcc, v63, v62
	s_and_b64 vcc, s[8:9], vcc
	s_xor_b64 s[8:9], s[68:69], -1
	v_cndmask_b32_e64 v64, v65, 7, vcc
	v_cndmask_b32_e32 v62, v62, v63, vcc
	v_cmp_ne_u32_e32 vcc, 8, v94
	s_and_b64 s[8:9], s[8:9], vcc
	v_cmp_gt_f32_e32 vcc, v60, v62
	s_and_b64 vcc, s[8:9], vcc
	s_xor_b64 s[8:9], s[66:67], -1
	v_cndmask_b32_e64 v63, v64, 8, vcc
	v_cndmask_b32_e32 v60, v62, v60, vcc
	v_cmp_ne_u32_e32 vcc, 9, v94
	s_and_b64 s[8:9], s[8:9], vcc
	v_cmp_gt_f32_e32 vcc, v61, v60
	s_and_b64 vcc, s[8:9], vcc
	s_xor_b64 s[8:9], s[64:65], -1
	v_cndmask_b32_e64 v62, v63, 9, vcc
	v_cndmask_b32_e32 v60, v60, v61, vcc
	v_cmp_ne_u32_e32 vcc, 10, v94
	s_and_b64 s[8:9], s[8:9], vcc
	v_cmp_gt_f32_e32 vcc, v58, v60
	s_and_b64 vcc, s[8:9], vcc
	s_xor_b64 s[8:9], s[62:63], -1
	v_cndmask_b32_e64 v61, v62, 10, vcc
	v_cndmask_b32_e32 v58, v60, v58, vcc
	v_cmp_ne_u32_e32 vcc, 11, v94
	s_and_b64 s[8:9], s[8:9], vcc
	v_cmp_gt_f32_e32 vcc, v59, v58
	s_and_b64 vcc, s[8:9], vcc
	s_xor_b64 s[8:9], s[60:61], -1
	v_cndmask_b32_e64 v60, v61, 11, vcc
	v_cndmask_b32_e32 v58, v58, v59, vcc
	v_cmp_ne_u32_e32 vcc, 12, v94
	s_and_b64 s[8:9], s[8:9], vcc
	v_cmp_gt_f32_e32 vcc, v14, v58
	s_and_b64 vcc, s[8:9], vcc
	s_xor_b64 s[8:9], s[58:59], -1
	v_cndmask_b32_e64 v59, v60, 12, vcc
	v_cndmask_b32_e32 v14, v58, v14, vcc
	v_cmp_ne_u32_e32 vcc, 13, v94
	s_and_b64 s[8:9], s[8:9], vcc
	v_cmp_gt_f32_e32 vcc, v15, v14
	s_and_b64 vcc, s[8:9], vcc
	s_xor_b64 s[8:9], s[56:57], -1
	v_cndmask_b32_e64 v58, v59, 13, vcc
	v_cndmask_b32_e32 v14, v14, v15, vcc
	v_cmp_ne_u32_e32 vcc, 14, v94
	s_and_b64 s[8:9], s[8:9], vcc
	v_cmp_gt_f32_e32 vcc, v12, v14
	s_and_b64 vcc, s[8:9], vcc
	s_xor_b64 s[8:9], s[54:55], -1
	v_cndmask_b32_e64 v15, v58, 14, vcc
	v_cndmask_b32_e32 v12, v14, v12, vcc
	v_cmp_ne_u32_e32 vcc, 15, v94
	s_and_b64 s[8:9], s[8:9], vcc
	v_cmp_gt_f32_e32 vcc, v13, v12
	s_and_b64 vcc, s[8:9], vcc
	s_xor_b64 s[8:9], s[52:53], -1
	v_cndmask_b32_e64 v14, v15, 15, vcc
	v_cndmask_b32_e32 v12, v12, v13, vcc
	v_cmp_ne_u32_e32 vcc, 16, v94
	s_and_b64 s[8:9], s[8:9], vcc
	v_cmp_gt_f32_e32 vcc, v72, v12
	s_and_b64 vcc, s[8:9], vcc
	s_xor_b64 s[8:9], s[50:51], -1
	v_cndmask_b32_e64 v13, v14, 16, vcc
	v_cndmask_b32_e32 v12, v12, v72, vcc
	v_cmp_ne_u32_e32 vcc, 17, v94
	s_and_b64 s[8:9], s[8:9], vcc
	v_cmp_gt_f32_e32 vcc, v73, v12
	s_and_b64 vcc, s[8:9], vcc
	s_xor_b64 s[8:9], s[48:49], -1
	v_cndmask_b32_e64 v13, v13, 17, vcc
	v_cndmask_b32_e32 v12, v12, v73, vcc
	v_cmp_ne_u32_e32 vcc, 18, v94
	s_and_b64 s[8:9], s[8:9], vcc
	v_cmp_gt_f32_e32 vcc, v70, v12
	s_and_b64 vcc, s[8:9], vcc
	s_xor_b64 s[8:9], s[46:47], -1
	v_cndmask_b32_e64 v13, v13, 18, vcc
	v_cndmask_b32_e32 v12, v12, v70, vcc
	v_cmp_ne_u32_e32 vcc, 19, v94
	s_and_b64 s[8:9], s[8:9], vcc
	v_cmp_gt_f32_e32 vcc, v71, v12
	s_and_b64 vcc, s[8:9], vcc
	s_xor_b64 s[8:9], s[44:45], -1
	v_cndmask_b32_e64 v13, v13, 19, vcc
	v_cndmask_b32_e32 v12, v12, v71, vcc
	v_cmp_ne_u32_e32 vcc, 20, v94
	s_and_b64 s[8:9], s[8:9], vcc
	v_cmp_gt_f32_e32 vcc, v10, v12
	s_and_b64 vcc, s[8:9], vcc
	s_xor_b64 s[8:9], s[42:43], -1
	v_cndmask_b32_e64 v13, v13, 20, vcc
	v_cndmask_b32_e32 v10, v12, v10, vcc
	v_cmp_ne_u32_e32 vcc, 21, v94
	s_and_b64 s[8:9], s[8:9], vcc
	v_cmp_gt_f32_e32 vcc, v11, v10
	s_and_b64 vcc, s[8:9], vcc
	s_xor_b64 s[8:9], s[40:41], -1
	v_cndmask_b32_e64 v12, v13, 21, vcc
	v_cndmask_b32_e32 v10, v10, v11, vcc
	v_cmp_ne_u32_e32 vcc, 22, v94
	s_and_b64 s[8:9], s[8:9], vcc
	v_cmp_gt_f32_e32 vcc, v8, v10
	s_and_b64 vcc, s[8:9], vcc
	s_xor_b64 s[8:9], s[38:39], -1
	v_cndmask_b32_e64 v11, v12, 22, vcc
	v_cndmask_b32_e32 v8, v10, v8, vcc
	v_cmp_ne_u32_e32 vcc, 23, v94
	s_and_b64 s[8:9], s[8:9], vcc
	v_cmp_gt_f32_e32 vcc, v9, v8
	s_and_b64 vcc, s[8:9], vcc
	s_xor_b64 s[8:9], s[36:37], -1
	v_cndmask_b32_e64 v10, v11, 23, vcc
	v_cndmask_b32_e32 v8, v8, v9, vcc
	v_cmp_ne_u32_e32 vcc, 24, v94
	s_and_b64 s[8:9], s[8:9], vcc
	v_cmp_gt_f32_e32 vcc, v6, v8
	s_and_b64 vcc, s[8:9], vcc
	s_xor_b64 s[8:9], s[22:23], -1
	v_cndmask_b32_e64 v9, v10, 24, vcc
	v_cndmask_b32_e32 v6, v8, v6, vcc
	v_cmp_ne_u32_e32 vcc, 25, v94
	s_and_b64 s[8:9], s[8:9], vcc
	v_cmp_gt_f32_e32 vcc, v7, v6
	s_and_b64 vcc, s[8:9], vcc
	s_xor_b64 s[8:9], s[20:21], -1
	v_cndmask_b32_e64 v8, v9, 25, vcc
	v_cndmask_b32_e32 v6, v6, v7, vcc
	v_cmp_ne_u32_e32 vcc, 26, v94
	s_and_b64 s[8:9], s[8:9], vcc
	v_cmp_gt_f32_e32 vcc, v4, v6
	s_and_b64 vcc, s[8:9], vcc
	s_xor_b64 s[8:9], s[18:19], -1
	v_cndmask_b32_e64 v7, v8, 26, vcc
	v_cndmask_b32_e32 v4, v6, v4, vcc
	v_cmp_ne_u32_e32 vcc, 27, v94
	s_and_b64 s[8:9], s[8:9], vcc
	v_cmp_gt_f32_e32 vcc, v5, v4
	s_and_b64 vcc, s[8:9], vcc
	s_xor_b64 s[8:9], s[16:17], -1
	v_cndmask_b32_e64 v6, v7, 27, vcc
	v_cndmask_b32_e32 v4, v4, v5, vcc
	v_cmp_ne_u32_e32 vcc, 28, v94
	s_and_b64 s[8:9], s[8:9], vcc
	v_cmp_gt_f32_e32 vcc, v2, v4
	s_and_b64 vcc, s[8:9], vcc
	s_xor_b64 s[8:9], s[14:15], -1
	v_cndmask_b32_e64 v5, v6, 28, vcc
	v_cndmask_b32_e32 v2, v4, v2, vcc
	v_cmp_ne_u32_e32 vcc, 29, v94
	s_and_b64 s[8:9], s[8:9], vcc
	v_cmp_gt_f32_e32 vcc, v3, v2
	s_and_b64 vcc, s[8:9], vcc
	s_xor_b64 s[8:9], s[12:13], -1
	v_cndmask_b32_e64 v4, v5, 29, vcc
	v_cndmask_b32_e32 v2, v2, v3, vcc
	v_cmp_ne_u32_e32 vcc, 30, v94
	s_and_b64 s[8:9], s[8:9], vcc
	v_cmp_gt_f32_e32 vcc, v0, v2
	s_and_b64 vcc, s[8:9], vcc
	s_xor_b64 s[8:9], s[10:11], -1
	v_cndmask_b32_e64 v3, v4, 30, vcc
	v_cndmask_b32_e32 v0, v2, v0, vcc
	v_cmp_ne_u32_e32 vcc, 31, v94
	s_and_b64 s[8:9], s[8:9], vcc
	v_cmp_gt_f32_e32 vcc, v1, v0
	s_and_b64 vcc, s[8:9], vcc
	v_readlane_b32 s46, v254, 34
	v_cndmask_b32_e32 v0, v0, v1, vcc
	v_sub_f32_e32 v1, v92, v90
	v_cndmask_b32_e64 v2, v3, 31, vcc
	v_mul_f32_e32 v1, 0x3fb8aa3b, v1
	v_sub_f32_e32 v3, v93, v90
	v_exp_f32_e32 v1, v1
	v_mul_f32_e32 v3, 0x3fb8aa3b, v3
	v_sub_f32_e32 v0, v0, v90
	v_exp_f32_e32 v3, v3
	v_mul_f32_e32 v0, 0x3fb8aa3b, v0
	v_exp_f32_e32 v0, v0
	v_add_f32_e32 v4, 1.0, v1
	v_add_f32_e32 v4, v4, v3
	s_movk_i32 s83, 0x600
	v_add_f32_e32 v4, v4, v0
	v_div_scale_f32 v5, s[8:9], v4, v4, 1.0
	v_rcp_f32_e32 v6, v5
	v_readlane_b32 s79, v254, 33
	v_readlane_b32 s76, v254, 29
	v_readlane_b32 s75, v254, 28
	v_fma_f32 v7, -v5, v6, 1.0
	v_fmac_f32_e32 v6, v7, v6
	v_div_scale_f32 v7, vcc, 1.0, v4, 1.0
	v_mul_f32_e32 v8, v7, v6
	v_fma_f32 v9, -v5, v8, v7
	v_fmac_f32_e32 v8, v9, v6
	v_fma_f32 v5, -v5, v8, v7
	v_div_fmas_f32 v5, v5, v6, v8
	v_div_fixup_f32 v4, v5, v4, 1.0
	v_lshl_add_u32 v5, v55, 2, s86
	ds_add_rtn_u32 v5, v5, v239
	v_mul_f32_e32 v1, v1, v4
	v_mul_f32_e32 v3, v3, v4
	v_mul_f32_e32 v0, v0, v4
	ds_write_b32 v74, v55
	s_waitcnt lgkmcnt(1)
	ds_write_b32 v75, v5
	ds_write_b32 v76, v4
	v_lshl_add_u32 v4, v91, 2, s86
	ds_add_rtn_u32 v4, v4, v239
	ds_write_b32 v77, v91
	s_waitcnt lgkmcnt(1)
	ds_write_b32 v78, v4
	ds_write_b32 v79, v1
	v_lshl_add_u32 v1, v94, 2, s86
	ds_add_rtn_u32 v1, v1, v239
	ds_write_b32 v80, v94
	s_waitcnt lgkmcnt(1)
	ds_write_b32 v81, v1
	ds_write_b32 v82, v3
	v_lshl_add_u32 v1, v2, 2, s86
	ds_add_rtn_u32 v1, v1, v239
	v_readlane_b32 s47, v254, 35
	v_readlane_b32 s44, v254, 38
	v_readlane_b32 s77, v254, 30
	ds_write_b32 v83, v2
	s_waitcnt lgkmcnt(1)
	ds_write_b32 v84, v1
	ds_write_b32 v85, v0
